# differential-attention writeback: gate rows of the unit touched into L2 by two loads per wave before the eight serialized row groups
# speedup vs baseline: 1.0059x; 1.0059x over previous
; #define INP(k) launder_p(args.in[k])
; __global__ void __launch_bounds__(NWAVES * 64, 2) mega_fwd(Args args) {
;     ...
;                             const float* q1 = INP(6) + l * 128; const float* k1 = INP(7) + l * 128; const float* q2 = INP(8) + l * 128; const float* k2 = INP(9) + l * 128;
;                             const float s1 = wave_sum(q1[lane_p] * k1[lane_p] + q1[lane_p + 64] * k1[lane_p + 64]), s2 = wave_sum(q2[lane_p] * k2[lane_p] + q2[lane_p + 64] * k2[lane_p + 64]);
;                             const float lam = expf(s1) - expf(s2) + lam_init;
;                             asm volatile("s_waitcnt vmcnt(0)" ::: "memory");
;                             { f32x4 t[16];
; #pragma unroll
;                               for (int r = 0; r < 16; ++r) t[r] = *(const f32x4*)(sp + r * 4);
;                               asm volatile("" ::: "memory");
.LBB0_854:
	v_readlane_b32 s8, v252, 14
	v_readlane_b32 s9, v252, 15
	v_readlane_b32 s10, v252, 16
	v_readlane_b32 s11, v252, 17
	v_readlane_b32 s12, v252, 18
	v_readlane_b32 s13, v252, 19
	v_readlane_b32 s14, v252, 20
	v_readlane_b32 s15, v252, 21
	v_readlane_b32 s16, v252, 22
	v_readlane_b32 s17, v252, 23
	v_readlane_b32 s18, v252, 24
	v_readlane_b32 s19, v252, 25
	v_readlane_b32 s20, v252, 26
	v_readlane_b32 s21, v252, 27
	v_readlane_b32 s22, v252, 28
	v_readlane_b32 s23, v252, 29
	s_mov_b64 s[8:9], s[12:13]
	s_mov_b64 s[10:11], s[14:15]
	s_mov_b64 s[12:13], s[16:17]
	s_mov_b64 s[14:15], s[18:19]
	s_mov_b64 s[16:17], s[20:21]
	s_mov_b64 s[0:1], s[16:17]
	v_readlane_b32 s28, v254, 39
	s_mov_b64 s[18:19], s[22:23]
	v_readlane_b32 s29, v254, 40
	s_add_u32 s8, s0, s28
	s_addc_u32 s9, s1, s29
	s_mov_b64 s[0:1], s[18:19]
	s_add_u32 s10, s0, s28
	v_readlane_b32 s12, v252, 35
	v_ashrrev_i32_e32 v239, 31, v238
	v_lshrrev_b64 v[132:133], 2, v[68:69]
	s_addc_u32 s11, s1, s29
	v_readlane_b32 s13, v252, 36
	v_readlane_b32 s14, v252, 37
	v_readlane_b32 s15, v252, 38
	v_lshlrev_b64 v[68:69], 2, v[238:239]
	s_mov_b64 s[0:1], s[12:13]
	s_mov_b64 s[6:7], s[14:15]
	v_lshl_add_u64 v[70:71], s[8:9], 0, v[68:69]
	v_lshl_add_u64 v[74:75], s[10:11], 0, v[68:69]
	global_load_dword v72, v[70:71], off
	global_load_dword v76, v[74:75], off
	global_load_dword v73, v[70:71], off offset:256
	global_load_dword v77, v[74:75], off offset:256
	v_and_b32_e32 v1, 64, v229
	s_add_u32 s0, s0, s28
	s_addc_u32 s1, s1, s29
	s_add_u32 s6, s6, s28
	s_addc_u32 s7, s7, s29
	s_mov_b32 s2, 0x42b17218
	v_mov_b32_e32 v134, v36
	v_mov_b32_e32 v135, v20
	v_readlane_b32 s16, v252, 39
	v_readlane_b32 s17, v252, 40
	v_readlane_b32 s18, v252, 41
	v_readlane_b32 s19, v252, 42
	v_readlane_b32 s20, v252, 43
	v_readlane_b32 s21, v252, 44
	v_readlane_b32 s22, v252, 45
	v_readlane_b32 s23, v252, 46
	v_readlane_b32 s24, v252, 47
	v_readlane_b32 s25, v252, 48
	v_readlane_b32 s26, v252, 49
	v_readlane_b32 s27, v252, 50
	s_waitcnt vmcnt(0)
	v_pk_mul_f32 v[70:71], v[72:73], v[76:77]
	s_nop 0
	v_add_f32_e32 v2, v70, v71
	v_add_u32_e32 v70, 64, v1
	v_xor_b32_e32 v1, 1, v229
	v_cmp_lt_i32_e32 vcc, v1, v70
	s_nop 1
	v_cndmask_b32_e32 v1, v229, v1, vcc
	v_lshlrev_b32_e32 v1, 2, v1
	ds_bpermute_b32 v71, v1, v2
	s_waitcnt lgkmcnt(0)
	v_add_f32_e32 v2, v2, v71
	v_xor_b32_e32 v71, 2, v229
	v_cmp_lt_i32_e32 vcc, v71, v70
	s_nop 1
	v_cndmask_b32_e32 v71, v229, v71, vcc
	v_lshlrev_b32_e32 v246, 2, v71
	ds_bpermute_b32 v71, v246, v2
	s_waitcnt lgkmcnt(0)
	v_add_f32_e32 v2, v2, v71
	v_xor_b32_e32 v71, 4, v229
	v_cmp_lt_i32_e32 vcc, v71, v70
	s_nop 1
	v_cndmask_b32_e32 v71, v229, v71, vcc
	v_lshlrev_b32_e32 v247, 2, v71
	ds_bpermute_b32 v71, v247, v2
	s_waitcnt lgkmcnt(0)
	v_add_f32_e32 v2, v2, v71
	v_xor_b32_e32 v71, 8, v229
	v_cmp_lt_i32_e32 vcc, v71, v70
	s_nop 1
	v_cndmask_b32_e32 v71, v229, v71, vcc
	v_lshlrev_b32_e32 v248, 2, v71
	ds_bpermute_b32 v71, v248, v2
	s_waitcnt lgkmcnt(0)
	v_add_f32_e32 v2, v2, v71
	v_xor_b32_e32 v71, 16, v229
	v_cmp_lt_i32_e32 vcc, v71, v70
	s_nop 1
	v_cndmask_b32_e32 v71, v229, v71, vcc
	v_lshlrev_b32_e32 v249, 2, v71
	ds_bpermute_b32 v71, v249, v2
	s_waitcnt lgkmcnt(0)
	v_add_f32_e32 v2, v2, v71
	v_xor_b32_e32 v71, 32, v229
	v_cmp_lt_i32_e32 vcc, v71, v70
	s_nop 1
	v_cndmask_b32_e32 v70, v229, v71, vcc
	v_lshlrev_b32_e32 v76, 2, v70
	ds_bpermute_b32 v70, v76, v2
	s_waitcnt lgkmcnt(0)
	v_add_f32_e32 v2, v2, v70
	v_lshl_add_u64 v[70:71], s[0:1], 0, v[68:69]
	v_lshl_add_u64 v[68:69], s[6:7], 0, v[68:69]
	global_load_dword v72, v[70:71], off
	global_load_dword v74, v[68:69], off
	global_load_dword v73, v[70:71], off offset:256
	global_load_dword v75, v[68:69], off offset:256
	s_mov_b32 s0, 0x3fb8aa3b
	s_mov_b32 s1, 0xc2ce8ed0
	v_cmp_ngt_f32_e32 vcc, s1, v2
	s_waitcnt vmcnt(0)
	v_readlane_b32 s6, v253, 50
	v_readlane_b32 s7, v253, 51
	s_waitcnt vmcnt(0)
	v_pk_mul_f32 v[68:69], v[72:73], v[74:75]
	s_nop 0
	v_add_f32_e32 v68, v68, v69
	ds_bpermute_b32 v69, v1, v68
	s_waitcnt lgkmcnt(0)
	v_add_f32_e32 v68, v68, v69
	ds_bpermute_b32 v69, v246, v68
	s_waitcnt lgkmcnt(0)
	v_add_f32_e32 v68, v68, v69
	ds_bpermute_b32 v69, v247, v68
	s_waitcnt lgkmcnt(0)
	v_add_f32_e32 v68, v68, v69
	ds_bpermute_b32 v69, v248, v68
	s_waitcnt lgkmcnt(0)
	v_add_f32_e32 v68, v68, v69
	ds_bpermute_b32 v69, v249, v68
	s_waitcnt lgkmcnt(0)
	v_add_f32_e32 v68, v68, v69
	ds_bpermute_b32 v69, v76, v68
	s_waitcnt lgkmcnt(0)
	v_add_f32_e32 v68, v68, v69
	v_mul_f32_e32 v69, 0x3fb8aa3b, v2
	v_fma_f32 v70, v2, s0, -v69
	v_rndne_f32_e32 v71, v69
	v_fmac_f32_e32 v70, 0x32a5705f, v2
	v_sub_f32_e32 v69, v69, v71
	v_add_f32_e32 v69, v69, v70
	v_exp_f32_e32 v69, v69
	v_cvt_i32_f32_e32 v70, v71
	v_ldexp_f32 v69, v69, v70
	v_cndmask_b32_e32 v69, 0, v69, vcc
	v_cmp_nlt_f32_e32 vcc, s2, v2
	s_nop 1
	v_cndmask_b32_e32 v2, v243, v69, vcc
	v_mul_f32_e32 v69, 0x3fb8aa3b, v68
	v_fma_f32 v70, v68, s0, -v69
	v_rndne_f32_e32 v71, v69
	v_fmac_f32_e32 v70, 0x32a5705f, v68
	v_sub_f32_e32 v69, v69, v71
	v_add_f32_e32 v69, v69, v70
	v_exp_f32_e32 v69, v69
	v_cvt_i32_f32_e32 v70, v71
	v_cmp_ngt_f32_e32 vcc, s1, v68
	v_readlane_b32 s0, v254, 28
	v_readlane_b32 s1, v254, 29
	v_ldexp_f32 v69, v69, v70
	v_cndmask_b32_e32 v69, 0, v69, vcc
	v_cmp_nlt_f32_e32 vcc, s2, v68
	v_lshl_add_u64 v[236:237], v[132:133], 2, s[0:1]
	s_mov_b64 s[0:1], -1
	v_cndmask_b32_e32 v68, v243, v69, vcc
	v_sub_f32_e32 v2, v2, v68
	global_load_dwordx4 v[80:83], v[234:235], off offset:-1024
	global_load_dwordx4 v[76:79], v[234:235], off offset:-2048
	global_load_dwordx4 v[72:75], v[234:235], off offset:-3072
	global_load_dwordx4 v[68:71], v[234:235], off offset:-4096
	global_load_dwordx4 v[96:99], v[234:235], off offset:3072
	global_load_dwordx4 v[92:95], v[234:235], off offset:2048
	global_load_dwordx4 v[88:91], v[234:235], off offset:1024
	global_load_dwordx4 v[84:87], v[234:235], off
	s_mov_b64 s[100:101], 0x2000
	v_lshl_add_u64 v[234:235], v[234:235], 0, s[100:101]
	global_load_dwordx4 v[112:115], v[234:235], off offset:-1024
	global_load_dwordx4 v[108:111], v[234:235], off offset:-2048
	global_load_dwordx4 v[104:107], v[234:235], off offset:-3072
	global_load_dwordx4 v[100:103], v[234:235], off offset:-4096
	global_load_dwordx4 v[128:131], v[234:235], off offset:3072
	global_load_dwordx4 v[124:127], v[234:235], off offset:2048
	global_load_dwordx4 v[120:123], v[234:235], off offset:1024
	global_load_dwordx4 v[116:119], v[234:235], off
	s_mov_b32 s100, 0xffffe000
	s_mov_b32 s101, -1
	v_lshl_add_u64 v[234:235], v[234:235], 0, s[100:101]
	v_add_f32_e32 v136, v203, v2
	v_mul_f32_e32 v2, v136, v202
	s_and_b64 vcc, exec, s[6:7]
	s_waitcnt vmcnt(12)
; __global__ void __launch_bounds__(NWAVES * 64, 2) mega_fwd(Args args) {
;     ...
;                               for (int r = 0; r < 16; ++r) { const float a_ = lam * rli[r];
; #pragma unroll
;                                   for (int d0 = 0; d0 < 4; ++d0) o[d0][r] = t[r][d0] - a_ * o[d0][r]; } }
;                             float* sq = S2 + (size_t)(wave * 64 + lane_p) * 64;
;                             if (vh == 0) {
	v_pk_fma_f32 v[68:69], v[2:3], v[134:135], v[68:69] op_sel_hi:[0,1,1] neg_lo:[1,0,0] neg_hi:[1,0,0]
	v_mov_b32_e32 v134, v52
	v_mov_b32_e32 v135, v4
	v_pk_fma_f32 v[70:71], v[2:3], v[134:135], v[70:71] op_sel_hi:[0,1,1] neg_lo:[1,0,0] neg_hi:[1,0,0]
	v_mul_f32_e32 v2, v136, v204
	v_mov_b32_e32 v134, v37
	v_mov_b32_e32 v135, v21
	v_pk_fma_f32 v[72:73], v[2:3], v[134:135], v[72:73] op_sel_hi:[0,1,1] neg_lo:[1,0,0] neg_hi:[1,0,0]
	v_mov_b32_e32 v134, v53
	v_mov_b32_e32 v135, v5
	v_pk_fma_f32 v[74:75], v[2:3], v[134:135], v[74:75] op_sel_hi:[0,1,1] neg_lo:[1,0,0] neg_hi:[1,0,0]
	v_mul_f32_e32 v2, v136, v206
	v_mov_b32_e32 v134, v38
	v_mov_b32_e32 v135, v22
	v_pk_fma_f32 v[76:77], v[2:3], v[134:135], v[76:77] op_sel_hi:[0,1,1] neg_lo:[1,0,0] neg_hi:[1,0,0]
	v_mov_b32_e32 v134, v54
	v_mov_b32_e32 v135, v6
	v_pk_fma_f32 v[78:79], v[2:3], v[134:135], v[78:79] op_sel_hi:[0,1,1] neg_lo:[1,0,0] neg_hi:[1,0,0]
	v_mul_f32_e32 v2, v136, v208
	v_mov_b32_e32 v134, v39
	v_mov_b32_e32 v135, v23
	v_pk_fma_f32 v[80:81], v[2:3], v[134:135], v[80:81] op_sel_hi:[0,1,1] neg_lo:[1,0,0] neg_hi:[1,0,0]
	v_mov_b32_e32 v134, v55
	v_mov_b32_e32 v135, v7
	v_pk_fma_f32 v[82:83], v[2:3], v[134:135], v[82:83] op_sel_hi:[0,1,1] neg_lo:[1,0,0] neg_hi:[1,0,0]
	v_mul_f32_e32 v2, v136, v210
	v_mov_b32_e32 v134, v40
	v_mov_b32_e32 v135, v24
	s_waitcnt vmcnt(8)
	v_pk_fma_f32 v[84:85], v[2:3], v[134:135], v[84:85] op_sel_hi:[0,1,1] neg_lo:[1,0,0] neg_hi:[1,0,0]
	v_mov_b32_e32 v134, v56
	v_mov_b32_e32 v135, v8
	v_pk_fma_f32 v[86:87], v[2:3], v[134:135], v[86:87] op_sel_hi:[0,1,1] neg_lo:[1,0,0] neg_hi:[1,0,0]
	v_mul_f32_e32 v2, v136, v212
	v_mov_b32_e32 v134, v41
	v_mov_b32_e32 v135, v25
	v_pk_fma_f32 v[88:89], v[2:3], v[134:135], v[88:89] op_sel_hi:[0,1,1] neg_lo:[1,0,0] neg_hi:[1,0,0]
	v_mov_b32_e32 v134, v57
	v_mov_b32_e32 v135, v9
	v_pk_fma_f32 v[90:91], v[2:3], v[134:135], v[90:91] op_sel_hi:[0,1,1] neg_lo:[1,0,0] neg_hi:[1,0,0]
	v_mul_f32_e32 v2, v136, v214
	v_mov_b32_e32 v134, v42
	v_mov_b32_e32 v135, v26
	v_pk_fma_f32 v[92:93], v[2:3], v[134:135], v[92:93] op_sel_hi:[0,1,1] neg_lo:[1,0,0] neg_hi:[1,0,0]
	v_mov_b32_e32 v134, v58
	v_mov_b32_e32 v135, v10
	v_pk_fma_f32 v[94:95], v[2:3], v[134:135], v[94:95] op_sel_hi:[0,1,1] neg_lo:[1,0,0] neg_hi:[1,0,0]
	v_mul_f32_e32 v2, v136, v216
	v_mov_b32_e32 v134, v43
	v_mov_b32_e32 v135, v27
	v_pk_fma_f32 v[96:97], v[2:3], v[134:135], v[96:97] op_sel_hi:[0,1,1] neg_lo:[1,0,0] neg_hi:[1,0,0]
	v_mov_b32_e32 v134, v59
	v_mov_b32_e32 v135, v11
	v_pk_fma_f32 v[98:99], v[2:3], v[134:135], v[98:99] op_sel_hi:[0,1,1] neg_lo:[1,0,0] neg_hi:[1,0,0]
	v_mul_f32_e32 v2, v136, v218
	v_mov_b32_e32 v134, v44
	v_mov_b32_e32 v135, v28
	s_waitcnt vmcnt(4)
	v_pk_fma_f32 v[100:101], v[2:3], v[134:135], v[100:101] op_sel_hi:[0,1,1] neg_lo:[1,0,0] neg_hi:[1,0,0]
	v_mov_b32_e32 v134, v60
	v_mov_b32_e32 v135, v12
	v_pk_fma_f32 v[102:103], v[2:3], v[134:135], v[102:103] op_sel_hi:[0,1,1] neg_lo:[1,0,0] neg_hi:[1,0,0]
	v_mul_f32_e32 v2, v136, v220
	v_mov_b32_e32 v134, v45
	v_mov_b32_e32 v135, v29
	v_pk_fma_f32 v[104:105], v[2:3], v[134:135], v[104:105] op_sel_hi:[0,1,1] neg_lo:[1,0,0] neg_hi:[1,0,0]
	v_mov_b32_e32 v134, v61
	v_mov_b32_e32 v135, v13
	v_pk_fma_f32 v[106:107], v[2:3], v[134:135], v[106:107] op_sel_hi:[0,1,1] neg_lo:[1,0,0] neg_hi:[1,0,0]
	v_mul_f32_e32 v2, v136, v222
	v_mov_b32_e32 v134, v46
	v_mov_b32_e32 v135, v30
	v_pk_fma_f32 v[108:109], v[2:3], v[134:135], v[108:109] op_sel_hi:[0,1,1] neg_lo:[1,0,0] neg_hi:[1,0,0]
	v_mov_b32_e32 v134, v62
	v_mov_b32_e32 v135, v14
	v_pk_fma_f32 v[110:111], v[2:3], v[134:135], v[110:111] op_sel_hi:[0,1,1] neg_lo:[1,0,0] neg_hi:[1,0,0]
	v_mul_f32_e32 v2, v136, v224
	v_mov_b32_e32 v134, v47
	v_mov_b32_e32 v135, v31
	v_pk_fma_f32 v[112:113], v[2:3], v[134:135], v[112:113] op_sel_hi:[0,1,1] neg_lo:[1,0,0] neg_hi:[1,0,0]
	v_mov_b32_e32 v134, v63
	v_mov_b32_e32 v135, v15
	v_pk_fma_f32 v[114:115], v[2:3], v[134:135], v[114:115] op_sel_hi:[0,1,1] neg_lo:[1,0,0] neg_hi:[1,0,0]
	v_mul_f32_e32 v2, v136, v226
	v_mov_b32_e32 v134, v48
	v_mov_b32_e32 v135, v32
	s_waitcnt vmcnt(0)
	v_pk_fma_f32 v[116:117], v[2:3], v[134:135], v[116:117] op_sel_hi:[0,1,1] neg_lo:[1,0,0] neg_hi:[1,0,0]
	v_mov_b32_e32 v134, v64
	v_mov_b32_e32 v135, v16
	v_pk_fma_f32 v[118:119], v[2:3], v[134:135], v[118:119] op_sel_hi:[0,1,1] neg_lo:[1,0,0] neg_hi:[1,0,0]
	v_mul_f32_e32 v2, v136, v228
	v_mov_b32_e32 v134, v49
	v_mov_b32_e32 v135, v33
	v_pk_fma_f32 v[120:121], v[2:3], v[134:135], v[120:121] op_sel_hi:[0,1,1] neg_lo:[1,0,0] neg_hi:[1,0,0]
	v_mov_b32_e32 v134, v65
	v_mov_b32_e32 v135, v17
	v_pk_fma_f32 v[122:123], v[2:3], v[134:135], v[122:123] op_sel_hi:[0,1,1] neg_lo:[1,0,0] neg_hi:[1,0,0]
	v_mul_f32_e32 v2, v136, v230
	v_mov_b32_e32 v134, v50
	v_mov_b32_e32 v135, v34
	v_pk_fma_f32 v[124:125], v[2:3], v[134:135], v[124:125] op_sel_hi:[0,1,1] neg_lo:[1,0,0] neg_hi:[1,0,0]
	v_mov_b32_e32 v134, v66
	v_mov_b32_e32 v135, v18
	v_pk_fma_f32 v[126:127], v[2:3], v[134:135], v[126:127] op_sel_hi:[0,1,1] neg_lo:[1,0,0] neg_hi:[1,0,0]
	v_mul_f32_e32 v2, v136, v232
	v_mov_b32_e32 v134, v51
	v_mov_b32_e32 v135, v35
	v_pk_fma_f32 v[128:129], v[2:3], v[134:135], v[128:129] op_sel_hi:[0,1,1] neg_lo:[1,0,0] neg_hi:[1,0,0]
	v_mov_b32_e32 v134, v67
	v_mov_b32_e32 v135, v19
	v_pk_fma_f32 v[130:131], v[2:3], v[134:135], v[130:131] op_sel_hi:[0,1,1] neg_lo:[1,0,0] neg_hi:[1,0,0]
	s_cbranch_vccz .LBB0_1112
; #define INP(k) launder_p(args.in[k])
; __global__ void __launch_bounds__(NWAVES * 64, 2) mega_fwd(Args args) {
;     ...
;                             } else { const float* subg = INP(10) + l * 256;
;                                 asm volatile("s_waitcnt vmcnt(0)" ::: "memory");
;                                 float sg[8];
; #pragma unroll
;                                 for (int i = 0; i < 8; ++i) sg[i] = subg[(i >> 2) * 128 + (i & 3) * 32 + r32];
;                                 { f32x4 t[16];
; #pragma unroll
;                                   for (int r = 0; r < 16; ++r) t[r] = *(const f32x4*)(sq + r * 4);
;                                   asm volatile("" ::: "memory");
; #pragma unroll
;                                   for (int r = 0; r < 16; ++r) { float ssq = 0.f;
; #pragma unroll
;                                       for (int d0 = 0; d0 < 4; ++d0) ssq += t[r][d0] * t[r][d0] + o[d0][r] * o[d0][r];
; #pragma unroll
;                                       for (int off = 1; off < 32; off <<= 1) ssq += __shfl_xor(ssq, off);
;                                       rli[r] = __builtin_amdgcn_rsqf(ssq * (1.0f / 256.0f) + RMS_EPS) * (1.0f - lam_init); } }
	v_readlane_b32 s8, v252, 35
	v_readlane_b32 s12, v252, 39
	v_readlane_b32 s13, v252, 40
	s_mov_b64 s[0:1], s[12:13]
	v_readlane_b32 s6, v254, 41
	v_and_b32_e32 v2, 31, v238
	v_readlane_b32 s7, v254, 42
	s_add_u32 s0, s0, s6
	s_addc_u32 s1, s1, s7
	s_waitcnt vmcnt(0)
	v_lshlrev_b32_e32 v132, 2, v2
	global_load_dword v245, v132, s[0:1]
	global_load_dword v244, v132, s[0:1] offset:128
	global_load_dword v239, v132, s[0:1] offset:256
	global_load_dword v217, v132, s[0:1] offset:384
	global_load_dword v213, v132, s[0:1] offset:512
	global_load_dword v211, v132, s[0:1] offset:640
	global_load_dword v209, v132, s[0:1] offset:768
	global_load_dword v197, v132, s[0:1] offset:896
	global_load_dwordx4 v[180:183], v[236:237], off offset:-1024
	global_load_dwordx4 v[184:187], v[236:237], off offset:-2048
	global_load_dwordx4 v[188:191], v[236:237], off offset:-3072
	global_load_dwordx4 v[192:195], v[236:237], off offset:-4096
	global_load_dwordx4 v[164:167], v[236:237], off offset:3072
	global_load_dwordx4 v[168:171], v[236:237], off offset:2048
	global_load_dwordx4 v[172:175], v[236:237], off offset:1024
	global_load_dwordx4 v[176:179], v[236:237], off
	s_mov_b64 s[100:101], 0x2000
	v_lshl_add_u64 v[236:237], v[236:237], 0, s[100:101]
	global_load_dwordx4 v[148:151], v[236:237], off offset:-1024
	global_load_dwordx4 v[152:155], v[236:237], off offset:-2048
	global_load_dwordx4 v[156:159], v[236:237], off offset:-3072
	global_load_dwordx4 v[160:163], v[236:237], off offset:-4096
	global_load_dwordx4 v[132:135], v[236:237], off offset:3072
	global_load_dwordx4 v[136:139], v[236:237], off offset:2048
	global_load_dwordx4 v[140:143], v[236:237], off offset:1024
	global_load_dwordx4 v[144:147], v[236:237], off
	s_mov_b32 s100, 0xffffe000
	s_mov_b32 s101, -1
	v_lshl_add_u64 v[236:237], v[236:237], 0, s[100:101]
	v_pk_mul_f32 v[250:251], v[68:69], v[68:69]
	v_readlane_b32 s11, v252, 38
	v_readlane_b32 s0, v254, 48
	v_readlane_b32 s11, v254, 24
	s_mov_b32 s8, 0xe800
	v_readlane_b32 s10, v252, 37
	s_mov_b64 s[12:13], 0x3800
	s_movk_i32 s10, 0x3000
	v_lshlrev_b32_e32 v2, 1, v2
	v_readlane_b32 s9, v252, 36
	v_readlane_b32 s14, v252, 41
	v_readlane_b32 s15, v252, 42
	v_readlane_b32 s16, v252, 43
	v_readlane_b32 s17, v252, 44
	v_readlane_b32 s18, v252, 45
	v_readlane_b32 s19, v252, 46
	v_readlane_b32 s20, v252, 47
	v_readlane_b32 s21, v252, 48
	v_readlane_b32 s22, v252, 49
	v_readlane_b32 s23, v252, 50
	v_lshrrev_b32_e32 v4, 2, v238
	v_lshl_add_u32 v5, s11, 5, v4
	v_add_u32_e32 v5, s0, v5
	v_readlane_b32 s100, v253, 48
	v_readlane_b32 s101, v253, 49
	v_and_b32_e32 v8, 3, v238
	v_lshlrev_b32_e32 v8, 7, v8
	v_mov_b32_e32 v9, 0
	v_mov_b64_e32 v[6:7], s[100:101]
	s_nop 0
	v_mad_i64_i32 v[6:7], s[100:101], v5, s8, v[6:7]
	v_lshl_add_u64 v[6:7], v[6:7], 0, v[8:9]
	v_readlane_b32 s100, v254, 49
	v_lshl_add_u64 v[6:7], v[6:7], 0, s[12:13]
	s_nop 1
	v_mov_b32_e32 v8, s100
	v_lshlrev_b32_e32 v8, 1, v8
	v_lshl_add_u64 v[6:7], v[6:7], 0, v[8:9]
	global_load_dword v10, v[6:7], off
	s_mov_b64 s[100:101], 0xe8000
	v_lshl_add_u64 v[6:7], v[6:7], 0, s[100:101]
	global_load_dword v11, v[6:7], off
	s_waitcnt vmcnt(14)
	v_fma_f32 v192, v192, v192, v250
	v_fmac_f32_e32 v251, v193, v193
	v_add_f32_e32 v215, v192, v251
	v_pk_mul_f32 v[192:193], v[70:71], v[70:71]
	s_nop 0
	v_fma_f32 v192, v194, v194, v192
	v_add_f32_e32 v192, v215, v192
	v_fmac_f32_e32 v193, v195, v195
	v_add_f32_e32 v192, v192, v193
	ds_bpermute_b32 v193, v1, v192
	s_waitcnt lgkmcnt(0)
	v_add_f32_e32 v192, v192, v193
	ds_bpermute_b32 v193, v246, v192
	s_waitcnt lgkmcnt(0)
	v_add_f32_e32 v192, v192, v193
	ds_bpermute_b32 v193, v247, v192
	s_waitcnt lgkmcnt(0)
	v_add_f32_e32 v192, v192, v193
	ds_bpermute_b32 v193, v248, v192
	s_waitcnt lgkmcnt(0)
	v_add_f32_e32 v192, v192, v193
	ds_bpermute_b32 v193, v249, v192
	s_waitcnt lgkmcnt(0)
	v_add_f32_e32 v192, v192, v193
	v_fmamk_f32 v192, v192, 0x3b800000, v221
	v_rsq_f32_e32 v192, v192
	s_nop 0
	v_mul_f32_e32 v215, v205, v192
	v_pk_mul_f32 v[192:193], v[72:73], v[72:73]
	s_nop 0
	v_fma_f32 v188, v188, v188, v192
	v_fmac_f32_e32 v193, v189, v189
	v_add_f32_e32 v192, v188, v193
	v_pk_mul_f32 v[188:189], v[74:75], v[74:75]
	s_nop 0
	v_fma_f32 v188, v190, v190, v188
	v_add_f32_e32 v188, v192, v188
	v_fmac_f32_e32 v189, v191, v191
	v_add_f32_e32 v188, v188, v189
	ds_bpermute_b32 v189, v1, v188
	s_waitcnt lgkmcnt(0)
	v_add_f32_e32 v188, v188, v189
	ds_bpermute_b32 v189, v246, v188
	s_waitcnt lgkmcnt(0)
	v_add_f32_e32 v188, v188, v189
	ds_bpermute_b32 v189, v247, v188
	s_waitcnt lgkmcnt(0)
	v_add_f32_e32 v188, v188, v189
	ds_bpermute_b32 v189, v248, v188
	s_waitcnt lgkmcnt(0)
	v_add_f32_e32 v251, v188, v189
	v_pk_mul_f32 v[188:189], v[76:77], v[76:77]
	ds_bpermute_b32 v223, v249, v251
	v_fma_f32 v184, v184, v184, v188
	v_fmac_f32_e32 v189, v185, v185
	v_add_f32_e32 v188, v184, v189
	v_pk_mul_f32 v[184:185], v[78:79], v[78:79]
	s_nop 0
	v_fma_f32 v184, v186, v186, v184
	v_add_f32_e32 v184, v188, v184
	v_fmac_f32_e32 v185, v187, v187
	v_add_f32_e32 v184, v184, v185
	ds_bpermute_b32 v185, v1, v184
	s_waitcnt lgkmcnt(0)
	v_add_f32_e32 v184, v184, v185
	ds_bpermute_b32 v185, v246, v184
	s_waitcnt lgkmcnt(0)
	v_add_f32_e32 v184, v184, v185
	ds_bpermute_b32 v185, v247, v184
	s_waitcnt lgkmcnt(0)
	v_add_f32_e32 v184, v184, v185
	ds_bpermute_b32 v185, v248, v184
	s_waitcnt lgkmcnt(0)
	v_add_f32_e32 v189, v184, v185
	v_pk_mul_f32 v[184:185], v[80:81], v[80:81]
	ds_bpermute_b32 v191, v249, v189
	v_fma_f32 v180, v180, v180, v184
	v_fmac_f32_e32 v185, v181, v181
	v_add_f32_e32 v184, v180, v185
	v_pk_mul_f32 v[180:181], v[82:83], v[82:83]
	s_nop 0
	v_fma_f32 v180, v182, v182, v180
	v_add_f32_e32 v180, v184, v180
	v_fmac_f32_e32 v181, v183, v183
	v_add_f32_e32 v180, v180, v181
	ds_bpermute_b32 v181, v1, v180
	s_waitcnt lgkmcnt(0)
; __global__ void __launch_bounds__(NWAVES * 64, 2) mega_fwd(Args args) {
;     ...
;                                   for (int r = 0; r < 16; ++r) { float ssq = 0.f;
; #pragma unroll
;                                       for (int d0 = 0; d0 < 4; ++d0) ssq += t[r][d0] * t[r][d0] + o[d0][r] * o[d0][r];
; #pragma unroll
;                                       for (int off = 1; off < 32; off <<= 1) ssq += __shfl_xor(ssq, off);
;                                       rli[r] = __builtin_amdgcn_rsqf(ssq * (1.0f / 256.0f) + RMS_EPS) * (1.0f - lam_init); } }
	v_add_f32_e32 v180, v180, v181
	ds_bpermute_b32 v181, v246, v180
	s_waitcnt lgkmcnt(0)
	v_add_f32_e32 v180, v180, v181
	ds_bpermute_b32 v181, v247, v180
	s_waitcnt lgkmcnt(0)
	v_add_f32_e32 v180, v180, v181
	ds_bpermute_b32 v181, v248, v180
	s_waitcnt lgkmcnt(0)
	v_add_f32_e32 v187, v180, v181
	v_pk_mul_f32 v[180:181], v[84:85], v[84:85]
	ds_bpermute_b32 v188, v249, v187
	s_waitcnt vmcnt(10)
	v_fma_f32 v176, v176, v176, v180
	v_fmac_f32_e32 v181, v177, v177
	v_add_f32_e32 v180, v176, v181
	v_pk_mul_f32 v[176:177], v[86:87], v[86:87]
	s_nop 0
	v_fma_f32 v176, v178, v178, v176
	v_add_f32_e32 v176, v180, v176
	v_fmac_f32_e32 v177, v179, v179
	v_add_f32_e32 v176, v176, v177
	ds_bpermute_b32 v177, v1, v176
	v_pk_mul_f32 v[178:179], v[88:89], v[88:89]
	s_waitcnt lgkmcnt(0)
	v_add_f32_e32 v176, v176, v177
	ds_bpermute_b32 v177, v246, v176
	v_fma_f32 v172, v172, v172, v178
	v_fmac_f32_e32 v179, v173, v173
	s_waitcnt lgkmcnt(0)
	v_add_f32_e32 v176, v176, v177
	ds_bpermute_b32 v177, v247, v176
	s_waitcnt lgkmcnt(0)
	v_add_f32_e32 v176, v176, v177
	ds_bpermute_b32 v177, v248, v176
	s_waitcnt lgkmcnt(0)
	v_add_f32_e32 v176, v176, v177
	v_add_f32_e32 v177, v172, v179
	v_pk_mul_f32 v[172:173], v[90:91], v[90:91]
	ds_bpermute_b32 v186, v249, v176
	v_fma_f32 v172, v174, v174, v172
	v_add_f32_e32 v172, v177, v172
	v_fmac_f32_e32 v173, v175, v175
	v_add_f32_e32 v172, v172, v173
	ds_bpermute_b32 v173, v1, v172
	v_pk_mul_f32 v[174:175], v[92:93], v[92:93]
	s_waitcnt lgkmcnt(0)
	v_add_f32_e32 v172, v172, v173
	ds_bpermute_b32 v173, v246, v172
	v_fma_f32 v168, v168, v168, v174
	v_fmac_f32_e32 v175, v169, v169
	s_waitcnt lgkmcnt(0)
	v_add_f32_e32 v172, v172, v173
	ds_bpermute_b32 v173, v247, v172
	s_waitcnt lgkmcnt(0)
	v_add_f32_e32 v172, v172, v173
	ds_bpermute_b32 v173, v248, v172
	s_waitcnt lgkmcnt(0)
	v_add_f32_e32 v173, v172, v173
	v_add_f32_e32 v172, v168, v175
	v_pk_mul_f32 v[168:169], v[94:95], v[94:95]
	ds_bpermute_b32 v250, v249, v173
	v_fma_f32 v168, v170, v170, v168
	v_add_f32_e32 v168, v172, v168
	v_fmac_f32_e32 v169, v171, v171
	v_add_f32_e32 v168, v168, v169
	ds_bpermute_b32 v169, v1, v168
	s_waitcnt lgkmcnt(0)
	v_add_f32_e32 v168, v168, v169
	ds_bpermute_b32 v169, v246, v168
	s_waitcnt lgkmcnt(0)
	v_add_f32_e32 v168, v168, v169
	ds_bpermute_b32 v169, v247, v168
	s_waitcnt lgkmcnt(0)
	v_add_f32_e32 v168, v168, v169
	ds_bpermute_b32 v169, v248, v168
	s_waitcnt lgkmcnt(0)
	v_add_f32_e32 v174, v168, v169
	v_pk_mul_f32 v[168:169], v[96:97], v[96:97]
	ds_bpermute_b32 v190, v249, v174
	v_fma_f32 v164, v164, v164, v168
	v_fmac_f32_e32 v169, v165, v165
	v_add_f32_e32 v168, v164, v169
	v_pk_mul_f32 v[164:165], v[98:99], v[98:99]
	s_nop 0
	v_fma_f32 v164, v166, v166, v164
	v_add_f32_e32 v164, v168, v164
	v_fmac_f32_e32 v165, v167, v167
	v_add_f32_e32 v164, v164, v165
	ds_bpermute_b32 v165, v1, v164
	s_waitcnt lgkmcnt(0)
	v_add_f32_e32 v164, v164, v165
	ds_bpermute_b32 v165, v246, v164
	s_waitcnt lgkmcnt(0)
	v_add_f32_e32 v164, v164, v165
	ds_bpermute_b32 v165, v247, v164
	s_waitcnt lgkmcnt(0)
	v_add_f32_e32 v164, v164, v165
	ds_bpermute_b32 v165, v248, v164
	s_waitcnt lgkmcnt(0)
	v_add_f32_e32 v175, v164, v165
	v_pk_mul_f32 v[164:165], v[100:101], v[100:101]
	ds_bpermute_b32 v185, v249, v175
	s_waitcnt vmcnt(6)
	v_fma_f32 v160, v160, v160, v164
	v_fmac_f32_e32 v165, v161, v161
	v_add_f32_e32 v164, v160, v165
	v_pk_mul_f32 v[160:161], v[102:103], v[102:103]
	s_nop 0
	v_fma_f32 v160, v162, v162, v160
	v_add_f32_e32 v160, v164, v160
	v_fmac_f32_e32 v161, v163, v163
	v_add_f32_e32 v160, v160, v161
	ds_bpermute_b32 v161, v1, v160
	s_waitcnt lgkmcnt(0)
	v_add_f32_e32 v160, v160, v161
	ds_bpermute_b32 v161, v246, v160
	s_waitcnt lgkmcnt(0)
	v_add_f32_e32 v160, v160, v161
	ds_bpermute_b32 v161, v247, v160
	s_waitcnt lgkmcnt(0)
	v_add_f32_e32 v160, v160, v161
	ds_bpermute_b32 v161, v248, v160
	s_waitcnt lgkmcnt(0)
	v_add_f32_e32 v168, v160, v161
	v_pk_mul_f32 v[160:161], v[104:105], v[104:105]
	ds_bpermute_b32 v180, v249, v168
	v_fma_f32 v156, v156, v156, v160
	v_fmac_f32_e32 v161, v157, v157
	v_add_f32_e32 v160, v156, v161
	v_pk_mul_f32 v[156:157], v[106:107], v[106:107]
	s_nop 0
	v_fma_f32 v156, v158, v158, v156
	v_add_f32_e32 v156, v160, v156
	v_fmac_f32_e32 v157, v159, v159
	v_add_f32_e32 v156, v156, v157
	ds_bpermute_b32 v157, v1, v156
	s_waitcnt lgkmcnt(0)
	v_add_f32_e32 v156, v156, v157
	ds_bpermute_b32 v157, v246, v156
	s_waitcnt lgkmcnt(0)
	v_add_f32_e32 v156, v156, v157
	ds_bpermute_b32 v157, v247, v156
	s_waitcnt lgkmcnt(0)
	v_add_f32_e32 v156, v156, v157
	ds_bpermute_b32 v157, v248, v156
	s_waitcnt lgkmcnt(0)
	v_add_f32_e32 v177, v156, v157
	v_pk_mul_f32 v[156:157], v[108:109], v[108:109]
	ds_bpermute_b32 v184, v249, v177
	v_fma_f32 v152, v152, v152, v156
	v_fmac_f32_e32 v157, v153, v153
	v_add_f32_e32 v156, v152, v157
	v_pk_mul_f32 v[152:153], v[110:111], v[110:111]
	s_nop 0
	v_fma_f32 v152, v154, v154, v152
	v_add_f32_e32 v152, v156, v152
	v_fmac_f32_e32 v153, v155, v155
	v_add_f32_e32 v152, v152, v153
	ds_bpermute_b32 v153, v1, v152
	s_waitcnt lgkmcnt(0)
	v_add_f32_e32 v152, v152, v153
	ds_bpermute_b32 v153, v246, v152
	s_waitcnt lgkmcnt(0)
	v_add_f32_e32 v152, v152, v153
	ds_bpermute_b32 v153, v247, v152
	s_waitcnt lgkmcnt(0)
	v_add_f32_e32 v152, v152, v153
	ds_bpermute_b32 v153, v248, v152
	s_waitcnt lgkmcnt(0)
	v_add_f32_e32 v178, v152, v153
	v_pk_mul_f32 v[152:153], v[112:113], v[112:113]
	ds_bpermute_b32 v183, v249, v178
	v_fma_f32 v148, v148, v148, v152
	v_fmac_f32_e32 v153, v149, v149
	v_add_f32_e32 v152, v148, v153
	v_pk_mul_f32 v[148:149], v[114:115], v[114:115]
	s_nop 0
	v_fma_f32 v148, v150, v150, v148
	v_add_f32_e32 v148, v152, v148
	v_fmac_f32_e32 v149, v151, v151
	v_add_f32_e32 v148, v148, v149
	ds_bpermute_b32 v149, v1, v148
	s_waitcnt lgkmcnt(0)
; __device__ __forceinline__ float bflo(unsigned w) { return __uint_as_float(w << 16); }
; __device__ __forceinline__ float bfhi(unsigned w) { return __uint_as_float(w & 0xffff0000u); }
; __device__ __forceinline__ unsigned pk2(float lo, float hi) { return f2bf(lo) | (f2bf(hi) << 16); }
; __device__ __forceinline__ int crow(int r, int hi) { return (r & 3) + 8 * (r >> 2) + 4 * hi; }
; __global__ void __launch_bounds__(NWAVES * 64, 2) mega_fwd(Args args) {
;     ...
;                                   for (int r = 0; r < 16; ++r) { float ssq = 0.f;
; #pragma unroll
;                                       for (int d0 = 0; d0 < 4; ++d0) ssq += t[r][d0] * t[r][d0] + o[d0][r] * o[d0][r];
; #pragma unroll
;                                       for (int off = 1; off < 32; off <<= 1) ssq += __shfl_xor(ssq, off);
;                                       rli[r] = __builtin_amdgcn_rsqf(ssq * (1.0f / 256.0f) + RMS_EPS) * (1.0f - lam_init); } }
; #pragma unroll
;                                 for (int hv = 0; hv < 2; ++hv)
; #pragma unroll
;                                   for (int rq = 0; rq < 4; ++rq) { unsigned zz[16]; f32x4 t[4];
;                                     int wv_ = wave; asm volatile("" : "+s"(wv_));
; #pragma unroll
;                                     for (int rr = 0; rr < 4; ++rr) { const int r = rq * 4 + rr; const bf16_t* zp = PROJ + (size_t)(b * SEQ + L * 256 + wv_ * 32 + att::crow(r, hi)) * NC + C_ZB + h * 256 + hv * 128 + (r32 & ~1);
; #pragma unroll
;                                         for (int d0 = 0; d0 < 4; ++d0) zz[rr * 4 + d0] = *(const unsigned*)(zp + d0 * 32);
;                                         if (hv == 0) t[rr] = *(const f32x4*)(sq + r * 4); else t[rr] = (f32x4){o[0][r], o[1][r], o[2][r], o[3][r]}; }
;                                     asm volatile("" ::: "memory");
; #pragma unroll
;                                     for (int rr = 0; rr < 4; ++rr) { const int r = rq * 4 + rr; bf16_t* yp = Y + (size_t)(b * SEQ + L * 256 + wv_ * 32 + att::crow(r, hi)) * YS + BW + h * 256 + hv * 128 + r32;
; #pragma unroll
;                                         for (int d0 = 0; d0 < 4; ++d0) { const float val = t[rr][d0] * rli[r] * sg[hv * 4 + d0], vn = __shfl_xor(val, 1);
;                                             if ((r32 & 1) == 0) *(unsigned*)(yp + d0 * 32) = pk2(val * bflo(zz[rr * 4 + d0]), vn * bfhi(zz[rr * 4 + d0])); } } }
	v_add_f32_e32 v148, v148, v149
	ds_bpermute_b32 v149, v246, v148
	s_waitcnt lgkmcnt(0)
	v_add_f32_e32 v148, v148, v149
	ds_bpermute_b32 v149, v247, v148
	s_waitcnt lgkmcnt(0)
	v_add_f32_e32 v148, v148, v149
	ds_bpermute_b32 v149, v248, v148
	s_waitcnt lgkmcnt(0)
	v_add_f32_e32 v179, v148, v149
	v_pk_mul_f32 v[148:149], v[116:117], v[116:117]
	ds_bpermute_b32 v182, v249, v179
	s_waitcnt vmcnt(2)
	v_fma_f32 v144, v144, v144, v148
	v_fmac_f32_e32 v149, v145, v145
	v_add_f32_e32 v148, v144, v149
	v_pk_mul_f32 v[144:145], v[118:119], v[118:119]
	v_mov_b32_e32 v149, v3
	v_fma_f32 v144, v146, v146, v144
	v_add_f32_e32 v144, v148, v144
	v_fmac_f32_e32 v145, v147, v147
	v_add_f32_e32 v144, v144, v145
	ds_bpermute_b32 v145, v1, v144
	s_waitcnt lgkmcnt(0)
	v_add_f32_e32 v144, v144, v145
	ds_bpermute_b32 v145, v246, v144
	s_waitcnt lgkmcnt(0)
	v_add_f32_e32 v144, v144, v145
	ds_bpermute_b32 v145, v247, v144
	s_waitcnt lgkmcnt(0)
	v_add_f32_e32 v144, v144, v145
	ds_bpermute_b32 v145, v248, v144
	s_waitcnt lgkmcnt(0)
	v_add_f32_e32 v172, v144, v145
	v_pk_mul_f32 v[144:145], v[120:121], v[120:121]
	ds_bpermute_b32 v181, v249, v172
	v_fma_f32 v140, v140, v140, v144
	v_fmac_f32_e32 v145, v141, v141
	v_add_f32_e32 v144, v140, v145
	v_pk_mul_f32 v[140:141], v[122:123], v[122:123]
	s_nop 0
	v_fma_f32 v140, v142, v142, v140
	v_add_f32_e32 v140, v144, v140
	v_fmac_f32_e32 v141, v143, v143
	v_add_f32_e32 v140, v140, v141
	ds_bpermute_b32 v141, v1, v140
	s_waitcnt lgkmcnt(0)
	v_add_f32_e32 v140, v140, v141
	ds_bpermute_b32 v141, v246, v140
	s_waitcnt lgkmcnt(0)
	v_add_f32_e32 v140, v140, v141
	ds_bpermute_b32 v141, v247, v140
	s_waitcnt lgkmcnt(0)
	v_add_f32_e32 v140, v140, v141
	ds_bpermute_b32 v141, v248, v140
	s_waitcnt lgkmcnt(0)
	v_add_f32_e32 v166, v140, v141
	v_pk_mul_f32 v[140:141], v[124:125], v[124:125]
	ds_bpermute_b32 v167, v249, v166
	v_fma_f32 v136, v136, v136, v140
	v_fmac_f32_e32 v141, v137, v137
	v_add_f32_e32 v140, v136, v141
	v_pk_mul_f32 v[136:137], v[126:127], v[126:127]
	s_nop 0
	v_fma_f32 v136, v138, v138, v136
	v_add_f32_e32 v136, v140, v136
	v_fmac_f32_e32 v137, v139, v139
	v_add_f32_e32 v136, v136, v137
	ds_bpermute_b32 v137, v1, v136
	s_waitcnt lgkmcnt(0)
	v_add_f32_e32 v136, v136, v137
	ds_bpermute_b32 v137, v246, v136
	s_waitcnt lgkmcnt(0)
	v_add_f32_e32 v136, v136, v137
	ds_bpermute_b32 v137, v247, v136
	s_waitcnt lgkmcnt(0)
	v_add_f32_e32 v136, v136, v137
	ds_bpermute_b32 v137, v248, v136
	s_waitcnt lgkmcnt(0)
	v_add_f32_e32 v163, v136, v137
	v_pk_mul_f32 v[136:137], v[128:129], v[128:129]
	ds_bpermute_b32 v164, v249, v163
	v_fma_f32 v132, v132, v132, v136
	v_fmac_f32_e32 v137, v133, v133
	v_add_f32_e32 v136, v132, v137
	v_pk_mul_f32 v[132:133], v[130:131], v[130:131]
	s_nop 0
	v_fma_f32 v132, v134, v134, v132
	v_add_f32_e32 v132, v136, v132
	v_fmac_f32_e32 v133, v135, v135
	v_add_f32_e32 v132, v132, v133
	ds_bpermute_b32 v133, v1, v132
	v_and_b32_e32 v134, 30, v238
	v_lshlrev_b32_e32 v148, 1, v134
	s_waitcnt lgkmcnt(0)
	v_add_f32_e32 v132, v132, v133
	ds_bpermute_b32 v133, v246, v132
	s_waitcnt lgkmcnt(0)
	v_add_f32_e32 v132, v132, v133
	ds_bpermute_b32 v133, v247, v132
	s_waitcnt lgkmcnt(0)
	v_add_f32_e32 v132, v132, v133
	ds_bpermute_b32 v133, v248, v132
	s_waitcnt lgkmcnt(0)
	v_add_f32_e32 v160, v132, v133
	v_ashrrev_i32_e32 v132, 3, v238
	v_and_b32_e32 v132, -4, v132
	v_add_u32_e32 v162, s0, v132
	s_mov_b32 s0, s11
	v_and_b32_e32 v132, 1, v238
	v_lshl_add_u32 v156, s0, 5, v162
	v_readlane_b32 s0, v253, 48
	v_readlane_b32 s1, v253, 49
	v_cmp_eq_u32_e64 s[6:7], 0, v132
	v_or_b32_e32 v154, 1, v156
	v_mov_b64_e32 v[158:159], s[0:1]
	v_mad_i64_i32 v[132:133], s[0:1], v156, s8, v[158:159]
	v_readlane_b32 s0, v254, 49
	s_lshl_b32 s2, s0, 1
	v_lshl_add_u64 v[132:133], v[132:133], 0, s[2:3]
	v_lshl_add_u64 v[132:133], v[132:133], 0, v[148:149]
	v_mad_i64_i32 v[150:151], s[0:1], v154, s8, v[158:159]
	v_lshl_add_u64 v[134:135], v[132:133], 0, s[12:13]
	v_add_co_u32_e32 v132, vcc, s10, v132
	v_lshl_add_u64 v[150:151], v[150:151], 0, s[2:3]
	s_nop 0
	v_addc_co_u32_e32 v133, vcc, 0, v133, vcc
	v_lshl_add_u64 v[150:151], v[150:151], 0, v[148:149]
	v_lshl_add_u64 v[152:153], v[150:151], 0, s[12:13]
	v_add_co_u32_e32 v150, vcc, s10, v150
	ds_bpermute_b32 v161, v249, v160
	s_nop 0
	v_addc_co_u32_e32 v151, vcc, 0, v151, vcc
	global_load_dword v192, v[132:133], off offset:2048
	global_load_dword v233, v[134:135], off offset:64
	global_load_dword v169, v[134:135], off offset:128
	global_load_dword v155, v[134:135], off offset:192
	s_nop 0
	global_load_dwordx4 v[132:135], v[236:237], off offset:-1024
	global_load_dwordx4 v[136:139], v[236:237], off offset:-2048
	global_load_dwordx4 v[140:143], v[236:237], off offset:-3072
	global_load_dwordx4 v[144:147], v[236:237], off offset:-4096
	global_load_dword v240, v[150:151], off offset:2048
	global_load_dword v249, v[152:153], off offset:64
	global_load_dword v170, v[152:153], off offset:128
	s_nop 0
	global_load_dword v153, v[152:153], off offset:192
	v_or_b32_e32 v152, 2, v156
	v_mad_i64_i32 v[150:151], s[0:1], v152, s8, v[158:159]
	v_lshl_add_u64 v[150:151], v[150:151], 0, s[2:3]
	v_lshl_add_u64 v[150:151], v[150:151], 0, v[148:149]
	v_lshl_add_u64 v[194:195], v[150:151], 0, s[12:13]
	v_add_co_u32_e32 v150, vcc, s10, v150
	v_ashrrev_i32_e32 v157, 31, v156
	s_nop 0
	v_addc_co_u32_e32 v151, vcc, 0, v151, vcc
	global_load_dword v248, v[150:151], off offset:2048
	global_load_dword v247, v[194:195], off offset:64
	global_load_dword v171, v[194:195], off offset:128
	s_nop 0
	global_load_dword v151, v[194:195], off offset:192
	v_or_b32_e32 v150, 3, v156
	v_mad_i64_i32 v[158:159], s[0:1], v150, s8, v[158:159]
	v_lshl_add_u64 v[158:159], v[158:159], 0, s[2:3]
	v_lshl_add_u64 v[158:159], v[158:159], 0, v[148:149]
	v_lshl_add_u64 v[194:195], v[158:159], 0, s[12:13]
	v_add_co_u32_e32 v158, vcc, s10, v158
	v_lshlrev_b64 v[156:157], 13, v[156:157]
	s_nop 0
	v_addc_co_u32_e32 v159, vcc, 0, v159, vcc
	global_load_dword v246, v[158:159], off offset:2048
	global_load_dword v238, v[194:195], off offset:64
	global_load_dword v165, v[194:195], off offset:128
	global_load_dword v149, v[194:195], off offset:192
	v_lshl_add_u64 v[156:157], s[4:5], 0, v[156:157]
	v_lshl_add_u64 v[156:157], v[156:157], 0, v[2:3]
	s_waitcnt vmcnt(12)
	v_mul_f32_e32 v144, v215, v144
	v_mul_f32_e32 v159, v144, v245
	ds_bpermute_b32 v158, v1, v159
	s_and_saveexec_b64 s[0:1], s[6:7]
	s_cbranch_execz .LBB0_857
	v_lshlrev_b32_e32 v193, 16, v192
	v_and_b32_e32 v192, 0xffff0000, v192
	s_waitcnt lgkmcnt(0)
	v_pk_mul_f32 v[158:159], v[158:159], v[192:193]
	s_nop 0
	v_and_b32_sdwa v144, v159, v227 dst_sel:DWORD dst_unused:UNUSED_PAD src0_sel:WORD_1 src1_sel:DWORD
	v_and_b32_sdwa v192, v158, v227 dst_sel:DWORD dst_unused:UNUSED_PAD src0_sel:WORD_1 src1_sel:DWORD
	v_add3_u32 v144, v159, v144, s97
	v_add3_u32 v158, v158, v192, s97
	v_lshrrev_b32_e32 v144, 16, v144
	v_and_or_b32 v144, v158, s66, v144
	global_store_dword v[156:157], v144, off offset:2048
